# grid barrier: the 17th and 25th arriver of each XCD issue an early L2 write-back so the last arriver's release flush is short
# speedup vs baseline: 1.0154x; 1.0035x over previous
.LBB0_73:
	s_or_b64 exec, exec, s[12:13]
	v_cvt_f32_u32_e32 v5, v3
	s_waitcnt vmcnt(0)
	v_readfirstlane_b32 s0, v4
	v_sub_u32_e32 v4, 0, v3
	v_rcp_iflag_f32_e32 v5, v5
	v_add_u32_e32 v6, s0, v2
	v_mul_f32_e32 v5, 0x4f7ffffe, v5
	v_cvt_u32_f32_e32 v5, v5
	v_mul_lo_u32 v2, v4, v5
	v_mul_hi_u32 v2, v5, v2
	v_add_u32_e32 v2, v5, v2
	v_mul_hi_u32 v2, v6, v2
	v_mul_lo_u32 v4, v2, v3
	v_sub_u32_e32 v4, v6, v4
	v_add_u32_e32 v5, 1, v2
	v_cmp_ge_u32_e32 vcc, v4, v3
	s_nop 1
	v_cndmask_b32_e32 v2, v2, v5, vcc
	v_sub_u32_e32 v5, v4, v3
	v_cndmask_b32_e32 v4, v4, v5, vcc
	v_add_u32_e32 v5, 1, v2
	v_cmp_ge_u32_e32 vcc, v4, v3
	v_add_u32_e32 v4, 1, v6
	s_nop 0
	v_cndmask_b32_e32 v2, v2, v5, vcc
	v_mul_lo_u32 v5, v3, v2
	v_add_u32_e32 v3, v5, v3
	v_cmp_ne_u32_e32 vcc, v4, v3
	s_and_saveexec_b64 s[0:1], vcc
	s_xor_b64 s[10:11], exec, s[0:1]
	s_cbranch_execz .LBB0_87
	v_readfirstlane_b32 s0, v6
	v_readfirstlane_b32 s1, v5
	v_readfirstlane_b32 vcc_lo, v3
	s_nop 3
	s_sub_u32 s0, s0, s1
	s_sub_u32 s1, vcc_lo, s1
	s_lshr_b32 vcc_lo, s1, 1
	s_cmp_eq_u32 s0, vcc_lo
	s_cbranch_scc1 .Lpf_do_0
	s_mul_i32 s1, s1, 3
	s_lshr_b32 s1, s1, 2
	s_cmp_lg_u32 s0, s1
	s_cbranch_scc1 .Lpf_skip_0
.Lpf_do_0:
	buffer_wbl2 sc1
.Lpf_skip_0:
	s_waitcnt lgkmcnt(0)
	v_mov_b32_e32 v1, 0x2000
	global_load_dword v1, v1, s[8:9] offset:1024 sc1
	s_add_u32 s16, s8, 0x2400
	s_addc_u32 s17, s9, 0
	s_waitcnt vmcnt(0)
	v_cmp_eq_u32_e32 vcc, v1, v2
	s_and_saveexec_b64 s[12:13], vcc
	s_cbranch_execz .LBB0_86
	v_readlane_b32 s0, v253, 4
	v_readlane_b32 s1, v253, 5
	s_add_u32 s14, s0, 0x4200
	s_addc_u32 s15, s1, 0
	s_mov_b32 s0, 1
	s_mov_b64 s[18:19], 0
	v_mov_b32_e32 v1, 0
	s_branch .LBB0_77

.LBB0_2258:
	s_or_b64 exec, exec, s[10:11]
	v_cvt_f32_u32_e32 v5, v3
	s_waitcnt vmcnt(0)
	v_readfirstlane_b32 s0, v4
	v_sub_u32_e32 v4, 0, v3
	v_rcp_iflag_f32_e32 v5, v5
	v_add_u32_e32 v6, s0, v2
	v_mul_f32_e32 v5, 0x4f7ffffe, v5
	v_cvt_u32_f32_e32 v5, v5
	v_mul_lo_u32 v2, v4, v5
	v_mul_hi_u32 v2, v5, v2
	v_add_u32_e32 v2, v5, v2
	v_mul_hi_u32 v2, v6, v2
	v_mul_lo_u32 v4, v2, v3
	v_sub_u32_e32 v4, v6, v4
	v_add_u32_e32 v5, 1, v2
	v_cmp_ge_u32_e32 vcc, v4, v3
	s_nop 1
	v_cndmask_b32_e32 v2, v2, v5, vcc
	v_sub_u32_e32 v5, v4, v3
	v_cndmask_b32_e32 v4, v4, v5, vcc
	v_add_u32_e32 v5, 1, v2
	v_cmp_ge_u32_e32 vcc, v4, v3
	v_add_u32_e32 v4, 1, v6
	s_nop 0
	v_cndmask_b32_e32 v2, v2, v5, vcc
	v_mul_lo_u32 v5, v3, v2
	v_add_u32_e32 v3, v5, v3
	v_cmp_ne_u32_e32 vcc, v4, v3
	s_and_saveexec_b64 s[0:1], vcc
	s_xor_b64 s[8:9], exec, s[0:1]
	s_cbranch_execz .LBB0_2272
	v_readfirstlane_b32 s0, v6
	v_readfirstlane_b32 s1, v5
	v_readfirstlane_b32 vcc_lo, v3
	s_nop 3
	s_sub_u32 s0, s0, s1
	s_sub_u32 s1, vcc_lo, s1
	s_lshr_b32 vcc_lo, s1, 1
	s_cmp_eq_u32 s0, vcc_lo
	s_cbranch_scc1 .Lpf_do_17
	s_mul_i32 s1, s1, 3
	s_lshr_b32 s1, s1, 2
	s_cmp_lg_u32 s0, s1
	s_cbranch_scc1 .Lpf_skip_17

.Lpf_skip_17:
	s_waitcnt lgkmcnt(0)
	v_mov_b32_e32 v1, 0x2000
	global_load_dword v1, v1, s[4:5] offset:1024 sc1
	s_add_u32 s14, s4, 0x2400
	s_addc_u32 s15, s5, 0
	s_waitcnt vmcnt(0)
	v_cmp_eq_u32_e32 vcc, v1, v2
	s_and_saveexec_b64 s[10:11], vcc
	s_cbranch_execz .LBB0_2271
	v_readlane_b32 s0, v253, 4
	v_readlane_b32 s1, v253, 5
	s_add_u32 s12, s0, 0x4200
	s_addc_u32 s13, s1, 0
	s_mov_b32 s0, 1
	s_mov_b64 s[16:17], 0
	v_mov_b32_e32 v1, 0
	s_branch .LBB0_2262
